# on top of foxpipe: grid-barrier and counter spin loops sleep 4 instead of 1 between polls (less polling traffic/power while stragglers finish)
# speedup vs baseline: 1.0061x; 1.0061x over previous
; __device__ __forceinline__ unsigned xb_ld(unsigned* p)              { return __hip_atomic_load(p, __ATOMIC_RELAXED, __HIP_MEMORY_SCOPE_AGENT); }
; __device__ __forceinline__ void xcd_barrier_complete(unsigned* bar, unsigned x, unsigned& nloc, unsigned& nx) {
;     ...
;     for (;;) {
;         sum = 0u; cnt = 0u; mine = 0u;
; #pragma unroll
;         for (unsigned j = 0; j < 16; ++j) { const unsigned c = xb_ld(&bar[XB_XCNT(j)]); sum += c; cnt += (c > 0u) ? 1u : 0u; mine = (j == x) ? c : mine; }
;         if (sum == G) break;
;         __builtin_amdgcn_s_sleep(1);
;         if ((++sp & 255u) == 0u) { if (xb_ld(&bar[XB_TMO])) break; if (sp > XB_SPIN_CAP) { atomicAdd(&bar[XB_TMO], 1u); break; } }
;     }
.LBB0_136:
	global_load_dword v16, v17, s[8:9] sc1
	global_load_dword v1, v17, s[10:11] sc1
	global_load_dword v2, v17, s[14:15] sc1
	global_load_dword v3, v17, s[36:37] sc1
	global_load_dword v4, v17, s[38:39] sc1
	global_load_dword v5, v17, s[40:41] sc1
	global_load_dword v6, v17, s[42:43] sc1
	global_load_dword v7, v17, s[48:49] sc1
	global_load_dword v8, v17, s[50:51] sc1
	global_load_dword v9, v17, s[56:57] sc1
	global_load_dword v10, v17, s[58:59] sc1
	global_load_dword v11, v17, s[60:61] sc1
	global_load_dword v12, v17, s[62:63] sc1
	global_load_dword v13, v17, s[64:65] sc1
	global_load_dword v14, v17, s[66:67] sc1
	global_load_dword v15, v17, s[68:69] sc1
	s_mov_b64 s[70:71], -1
	s_mov_b64 s[72:73], -1
	s_waitcnt vmcnt(14)
	v_add_u32_e32 v18, v1, v16
	s_waitcnt vmcnt(13)
	v_add_u32_e32 v18, v18, v2
	s_waitcnt vmcnt(12)
	v_add_u32_e32 v18, v18, v3
	s_waitcnt vmcnt(11)
	v_add_u32_e32 v18, v18, v4
	s_waitcnt vmcnt(10)
	v_add_u32_e32 v18, v18, v5
	s_waitcnt vmcnt(9)
	v_add_u32_e32 v18, v18, v6
	s_waitcnt vmcnt(8)
	v_add_u32_e32 v18, v18, v7
	s_waitcnt vmcnt(7)
	v_add_u32_e32 v18, v18, v8
	s_waitcnt vmcnt(6)
	v_add_u32_e32 v18, v18, v9
	s_waitcnt vmcnt(5)
	v_add_u32_e32 v18, v18, v10
	s_waitcnt vmcnt(4)
	v_add_u32_e32 v18, v18, v11
	s_waitcnt vmcnt(3)
	v_add_u32_e32 v18, v18, v12
	s_waitcnt vmcnt(2)
	v_add_u32_e32 v18, v18, v13
	s_waitcnt vmcnt(1)
	v_add_u32_e32 v18, v18, v14
	s_waitcnt vmcnt(0)
	v_add_u32_e32 v18, v18, v15
	v_cmp_eq_u32_e32 vcc, s3, v18
	s_cbranch_vccnz .LBB0_135
	s_and_b32 s35, s34, 0xff
	s_cmp_eq_u32 s35, 0
	s_mov_b64 s[74:75], -1
	s_sleep 4
	s_cbranch_scc1 .LBB0_140
	s_and_b64 vcc, exec, s[74:75]
	s_cbranch_vccz .LBB0_135

; __device__ __forceinline__ unsigned xb_ld(unsigned* p)              { return __hip_atomic_load(p, __ATOMIC_RELAXED, __HIP_MEMORY_SCOPE_AGENT); }
; __device__ __forceinline__ unsigned xb_add(unsigned* p, unsigned v) { return __hip_atomic_fetch_add(p, v, __ATOMIC_RELAXED, __HIP_MEMORY_SCOPE_AGENT); }
; #define XB_SPIN(cond, bar) do { unsigned _sp = 0; while (cond) { __builtin_amdgcn_s_sleep(1); \
;     if ((++_sp & 255u) == 0u) { if (xb_ld(&(bar)[XB_TMO])) break; if (_sp > XB_SPIN_CAP) { atomicAdd(&(bar)[XB_TMO], 1u); break; } } } } while (0)
; __device__ __forceinline__ void xcd_barrier(const XcdBarrier& b) {
;     ...
;             const unsigned og = xb_add(&bar[XB_TOP], 1u);
;             const unsigned tg = og / nx;
;             if (og + 1u == (tg + 1u) * nx) xb_add(&bar[XB_TOPGEN], 1u);
;             else XB_SPIN(xb_ld(&bar[XB_TOPGEN]) == tg, bar);
.LBB0_152:
	s_and_b32 s34, s3, 0xff
	s_mov_b64 s[42:43], -1
	s_cmp_lg_u32 s34, 0
	s_mov_b64 s[50:51], -1
	s_sleep 4
	s_cbranch_scc0 .LBB0_155
	s_and_b64 vcc, exec, s[50:51]
	s_cbranch_vccz .LBB0_151

; __device__ __forceinline__ unsigned xb_ld(unsigned* p)              { return __hip_atomic_load(p, __ATOMIC_RELAXED, __HIP_MEMORY_SCOPE_AGENT); }
; #define XB_SPIN(cond, bar) do { unsigned _sp = 0; while (cond) { __builtin_amdgcn_s_sleep(1); \
;     if ((++_sp & 255u) == 0u) { if (xb_ld(&(bar)[XB_TMO])) break; if (_sp > XB_SPIN_CAP) { atomicAdd(&(bar)[XB_TMO], 1u); break; } } } } while (0)
; __device__ __forceinline__ void xcd_barrier(const XcdBarrier& b) {
;     ...
;         } else {
;             XB_SPIN(xb_ld(&bar[XB_XGEN(b.x)]) == gen, bar);
.LBB0_169:
	s_and_b32 s34, s3, 0xff
	s_cmp_lg_u32 s34, 0
	s_mov_b64 s[48:49], -1
	s_sleep 4
	s_cbranch_scc0 .LBB0_172
	s_mov_b64 s[50:51], -1
	s_and_b64 vcc, exec, s[48:49]
	s_cbranch_vccz .LBB0_168

; __device__ __forceinline__ unsigned xb_ld(unsigned* p)              { return __hip_atomic_load(p, __ATOMIC_RELAXED, __HIP_MEMORY_SCOPE_AGENT); }
; __device__ __forceinline__ void xcd_barrier_complete(unsigned* bar, unsigned x, unsigned& nloc, unsigned& nx) {
;     ...
;     for (;;) {
;         sum = 0u; cnt = 0u; mine = 0u;
; #pragma unroll
;         for (unsigned j = 0; j < 16; ++j) { const unsigned c = xb_ld(&bar[XB_XCNT(j)]); sum += c; cnt += (c > 0u) ? 1u : 0u; mine = (j == x) ? c : mine; }
;         if (sum == G) break;
;         __builtin_amdgcn_s_sleep(1);
;         if ((++sp & 255u) == 0u) { if (xb_ld(&bar[XB_TMO])) break; if (sp > XB_SPIN_CAP) { atomicAdd(&bar[XB_TMO], 1u); break; } }
;     }
.LBB0_320:
	global_load_dword v16, v17, s[8:9] sc1
	global_load_dword v1, v17, s[10:11] sc1
	global_load_dword v2, v17, s[14:15] sc1
	global_load_dword v3, v17, s[36:37] sc1
	global_load_dword v4, v17, s[38:39] sc1
	global_load_dword v5, v17, s[40:41] sc1
	global_load_dword v6, v17, s[42:43] sc1
	global_load_dword v7, v17, s[44:45] sc1
	global_load_dword v8, v17, s[48:49] sc1
	global_load_dword v9, v17, s[50:51] sc1
	global_load_dword v10, v17, s[56:57] sc1
	global_load_dword v11, v17, s[58:59] sc1
	global_load_dword v12, v17, s[60:61] sc1
	global_load_dword v13, v17, s[62:63] sc1
	global_load_dword v14, v17, s[64:65] sc1
	global_load_dword v15, v17, s[66:67] sc1
	s_mov_b64 s[68:69], -1
	s_mov_b64 s[70:71], -1
	s_waitcnt vmcnt(14)
	v_add_u32_e32 v18, v1, v16
	s_waitcnt vmcnt(13)
	v_add_u32_e32 v18, v18, v2
	s_waitcnt vmcnt(12)
	v_add_u32_e32 v18, v18, v3
	s_waitcnt vmcnt(11)
	v_add_u32_e32 v18, v18, v4
	s_waitcnt vmcnt(10)
	v_add_u32_e32 v18, v18, v5
	s_waitcnt vmcnt(9)
	v_add_u32_e32 v18, v18, v6
	s_waitcnt vmcnt(8)
	v_add_u32_e32 v18, v18, v7
	s_waitcnt vmcnt(7)
	v_add_u32_e32 v18, v18, v8
	s_waitcnt vmcnt(6)
	v_add_u32_e32 v18, v18, v9
	s_waitcnt vmcnt(5)
	v_add_u32_e32 v18, v18, v10
	s_waitcnt vmcnt(4)
	v_add_u32_e32 v18, v18, v11
	s_waitcnt vmcnt(3)
	v_add_u32_e32 v18, v18, v12
	s_waitcnt vmcnt(2)
	v_add_u32_e32 v18, v18, v13
	s_waitcnt vmcnt(1)
	v_add_u32_e32 v18, v18, v14
	s_waitcnt vmcnt(0)
	v_add_u32_e32 v18, v18, v15
	v_cmp_eq_u32_e32 vcc, s3, v18
	s_cbranch_vccnz .LBB0_319
	s_and_b32 s35, s34, 0xff
	s_cmp_eq_u32 s35, 0
	s_mov_b64 s[72:73], -1
	s_sleep 4
	s_cbranch_scc1 .LBB0_324
	s_and_b64 vcc, exec, s[72:73]
	s_cbranch_vccz .LBB0_319

; __device__ __forceinline__ unsigned xb_ld(unsigned* p)              { return __hip_atomic_load(p, __ATOMIC_RELAXED, __HIP_MEMORY_SCOPE_AGENT); }
; __device__ __forceinline__ unsigned xb_add(unsigned* p, unsigned v) { return __hip_atomic_fetch_add(p, v, __ATOMIC_RELAXED, __HIP_MEMORY_SCOPE_AGENT); }
; #define XB_SPIN(cond, bar) do { unsigned _sp = 0; while (cond) { __builtin_amdgcn_s_sleep(1); \
;     if ((++_sp & 255u) == 0u) { if (xb_ld(&(bar)[XB_TMO])) break; if (_sp > XB_SPIN_CAP) { atomicAdd(&(bar)[XB_TMO], 1u); break; } } } } while (0)
; __device__ __forceinline__ void xcd_barrier(const XcdBarrier& b) {
;     ...
;             const unsigned og = xb_add(&bar[XB_TOP], 1u);
;             const unsigned tg = og / nx;
;             if (og + 1u == (tg + 1u) * nx) xb_add(&bar[XB_TOPGEN], 1u);
;             else XB_SPIN(xb_ld(&bar[XB_TOPGEN]) == tg, bar);
.LBB0_336:
	s_and_b32 s34, s3, 0xff
	s_mov_b64 s[42:43], -1
	s_cmp_lg_u32 s34, 0
	s_mov_b64 s[48:49], -1
	s_sleep 4
	s_cbranch_scc0 .LBB0_339
	s_and_b64 vcc, exec, s[48:49]
	s_cbranch_vccz .LBB0_335

; __device__ __forceinline__ unsigned xb_ld(unsigned* p)              { return __hip_atomic_load(p, __ATOMIC_RELAXED, __HIP_MEMORY_SCOPE_AGENT); }
; #define XB_SPIN(cond, bar) do { unsigned _sp = 0; while (cond) { __builtin_amdgcn_s_sleep(1); \
;     if ((++_sp & 255u) == 0u) { if (xb_ld(&(bar)[XB_TMO])) break; if (_sp > XB_SPIN_CAP) { atomicAdd(&(bar)[XB_TMO], 1u); break; } } } } while (0)
; __device__ __forceinline__ void xcd_barrier(const XcdBarrier& b) {
;     ...
;         } else {
;             XB_SPIN(xb_ld(&bar[XB_XGEN(b.x)]) == gen, bar);
.LBB0_353:
	s_and_b32 s34, s3, 0xff
	s_cmp_lg_u32 s34, 0
	s_mov_b64 s[44:45], -1
	s_sleep 4
	s_cbranch_scc0 .LBB0_356
	s_mov_b64 s[48:49], -1
	s_and_b64 vcc, exec, s[44:45]
	s_cbranch_vccz .LBB0_352

; __device__ __forceinline__ unsigned xb_ld(unsigned* p)              { return __hip_atomic_load(p, __ATOMIC_RELAXED, __HIP_MEMORY_SCOPE_AGENT); }
; __device__ __forceinline__ void xcd_barrier_complete(unsigned* bar, unsigned x, unsigned& nloc, unsigned& nx) {
;     ...
;     for (;;) {
;         sum = 0u; cnt = 0u; mine = 0u;
; #pragma unroll
;         for (unsigned j = 0; j < 16; ++j) { const unsigned c = xb_ld(&bar[XB_XCNT(j)]); sum += c; cnt += (c > 0u) ? 1u : 0u; mine = (j == x) ? c : mine; }
;         if (sum == G) break;
;         __builtin_amdgcn_s_sleep(1);
;         if ((++sp & 255u) == 0u) { if (xb_ld(&bar[XB_TMO])) break; if (sp > XB_SPIN_CAP) { atomicAdd(&bar[XB_TMO], 1u); break; } }
;     }
.LBB0_723:
	global_load_dword v16, v17, s[8:9] sc1
	global_load_dword v1, v17, s[10:11] sc1
	global_load_dword v2, v17, s[14:15] sc1
	global_load_dword v3, v17, s[36:37] sc1
	global_load_dword v4, v17, s[38:39] sc1
	global_load_dword v5, v17, s[40:41] sc1
	global_load_dword v6, v17, s[42:43] sc1
	global_load_dword v7, v17, s[44:45] sc1
	global_load_dword v8, v17, s[46:47] sc1
	global_load_dword v9, v17, s[48:49] sc1
	global_load_dword v10, v17, s[50:51] sc1
	global_load_dword v11, v17, s[56:57] sc1
	global_load_dword v12, v17, s[58:59] sc1
	global_load_dword v13, v17, s[60:61] sc1
	global_load_dword v14, v17, s[62:63] sc1
	global_load_dword v15, v17, s[64:65] sc1
	s_mov_b64 s[66:67], -1
	s_mov_b64 s[68:69], -1
	s_waitcnt vmcnt(14)
	v_add_u32_e32 v18, v1, v16
	s_waitcnt vmcnt(13)
	v_add_u32_e32 v18, v18, v2
	s_waitcnt vmcnt(12)
	v_add_u32_e32 v18, v18, v3
	s_waitcnt vmcnt(11)
	v_add_u32_e32 v18, v18, v4
	s_waitcnt vmcnt(10)
	v_add_u32_e32 v18, v18, v5
	s_waitcnt vmcnt(9)
	v_add_u32_e32 v18, v18, v6
	s_waitcnt vmcnt(8)
	v_add_u32_e32 v18, v18, v7
	s_waitcnt vmcnt(7)
	v_add_u32_e32 v18, v18, v8
	s_waitcnt vmcnt(6)
	v_add_u32_e32 v18, v18, v9
	s_waitcnt vmcnt(5)
	v_add_u32_e32 v18, v18, v10
	s_waitcnt vmcnt(4)
	v_add_u32_e32 v18, v18, v11
	s_waitcnt vmcnt(3)
	v_add_u32_e32 v18, v18, v12
	s_waitcnt vmcnt(2)
	v_add_u32_e32 v18, v18, v13
	s_waitcnt vmcnt(1)
	v_add_u32_e32 v18, v18, v14
	s_waitcnt vmcnt(0)
	v_add_u32_e32 v18, v18, v15
	v_cmp_eq_u32_e32 vcc, s3, v18
	s_cbranch_vccnz .LBB0_722
	s_and_b32 s35, s34, 0xff
	s_cmp_eq_u32 s35, 0
	s_mov_b64 s[70:71], -1
	s_sleep 4
	s_cbranch_scc1 .LBB0_727
	s_and_b64 vcc, exec, s[70:71]
	s_cbranch_vccz .LBB0_722

; __device__ __forceinline__ unsigned xb_ld(unsigned* p)              { return __hip_atomic_load(p, __ATOMIC_RELAXED, __HIP_MEMORY_SCOPE_AGENT); }
; __device__ __forceinline__ unsigned xb_add(unsigned* p, unsigned v) { return __hip_atomic_fetch_add(p, v, __ATOMIC_RELAXED, __HIP_MEMORY_SCOPE_AGENT); }
; #define XB_SPIN(cond, bar) do { unsigned _sp = 0; while (cond) { __builtin_amdgcn_s_sleep(1); \
;     if ((++_sp & 255u) == 0u) { if (xb_ld(&(bar)[XB_TMO])) break; if (_sp > XB_SPIN_CAP) { atomicAdd(&(bar)[XB_TMO], 1u); break; } } } } while (0)
; __device__ __forceinline__ void xcd_barrier(const XcdBarrier& b) {
;     ...
;             const unsigned og = xb_add(&bar[XB_TOP], 1u);
;             const unsigned tg = og / nx;
;             if (og + 1u == (tg + 1u) * nx) xb_add(&bar[XB_TOPGEN], 1u);
;             else XB_SPIN(xb_ld(&bar[XB_TOPGEN]) == tg, bar);
.LBB0_739:
	s_and_b32 s34, s3, 0xff
	s_mov_b64 s[42:43], -1
	s_cmp_lg_u32 s34, 0
	s_mov_b64 s[46:47], -1
	s_sleep 4
	s_cbranch_scc0 .LBB0_742
	s_and_b64 vcc, exec, s[46:47]
	s_cbranch_vccz .LBB0_738

; __device__ __forceinline__ unsigned xb_ld(unsigned* p)              { return __hip_atomic_load(p, __ATOMIC_RELAXED, __HIP_MEMORY_SCOPE_AGENT); }
; #define XB_SPIN(cond, bar) do { unsigned _sp = 0; while (cond) { __builtin_amdgcn_s_sleep(1); \
;     if ((++_sp & 255u) == 0u) { if (xb_ld(&(bar)[XB_TMO])) break; if (_sp > XB_SPIN_CAP) { atomicAdd(&(bar)[XB_TMO], 1u); break; } } } } while (0)
; __device__ __forceinline__ void xcd_barrier(const XcdBarrier& b) {
;     ...
;         } else {
;             XB_SPIN(xb_ld(&bar[XB_XGEN(b.x)]) == gen, bar);
.LBB0_756:
	s_and_b32 s34, s3, 0xff
	s_cmp_lg_u32 s34, 0
	s_mov_b64 s[44:45], -1
	s_sleep 4
	s_cbranch_scc0 .LBB0_759
	s_mov_b64 s[46:47], -1
	s_and_b64 vcc, exec, s[44:45]
	s_cbranch_vccz .LBB0_755

; __device__ __forceinline__ unsigned xb_ld(unsigned* p)              { return __hip_atomic_load(p, __ATOMIC_RELAXED, __HIP_MEMORY_SCOPE_AGENT); }
; __device__ __forceinline__ void xcd_barrier_complete(unsigned* bar, unsigned x, unsigned& nloc, unsigned& nx) {
;     ...
;     for (;;) {
;         sum = 0u; cnt = 0u; mine = 0u;
; #pragma unroll
;         for (unsigned j = 0; j < 16; ++j) { const unsigned c = xb_ld(&bar[XB_XCNT(j)]); sum += c; cnt += (c > 0u) ? 1u : 0u; mine = (j == x) ? c : mine; }
;         if (sum == G) break;
;         __builtin_amdgcn_s_sleep(1);
;         if ((++sp & 255u) == 0u) { if (xb_ld(&bar[XB_TMO])) break; if (sp > XB_SPIN_CAP) { atomicAdd(&bar[XB_TMO], 1u); break; } }
;     }
.LBB0_958:
	global_load_dword v16, v17, s[6:7] sc1
	global_load_dword v1, v17, s[8:9] sc1
	global_load_dword v2, v17, s[10:11] sc1
	global_load_dword v3, v17, s[12:13] sc1
	global_load_dword v4, v17, s[14:15] sc1
	global_load_dword v5, v17, s[18:19] sc1
	global_load_dword v6, v17, s[36:37] sc1
	global_load_dword v7, v17, s[38:39] sc1
	global_load_dword v8, v17, s[40:41] sc1
	global_load_dword v9, v17, s[42:43] sc1
	global_load_dword v10, v17, s[44:45] sc1
	global_load_dword v11, v17, s[46:47] sc1
	global_load_dword v12, v17, s[48:49] sc1
	global_load_dword v13, v17, s[50:51] sc1
	global_load_dword v14, v17, s[56:57] sc1
	global_load_dword v15, v17, s[58:59] sc1
	s_mov_b64 s[60:61], -1
	s_mov_b64 s[62:63], -1
	s_waitcnt vmcnt(14)
	v_add_u32_e32 v18, v1, v16
	s_waitcnt vmcnt(13)
	v_add_u32_e32 v18, v18, v2
	s_waitcnt vmcnt(12)
	v_add_u32_e32 v18, v18, v3
	s_waitcnt vmcnt(11)
	v_add_u32_e32 v18, v18, v4
	s_waitcnt vmcnt(10)
	v_add_u32_e32 v18, v18, v5
	s_waitcnt vmcnt(9)
	v_add_u32_e32 v18, v18, v6
	s_waitcnt vmcnt(8)
	v_add_u32_e32 v18, v18, v7
	s_waitcnt vmcnt(7)
	v_add_u32_e32 v18, v18, v8
	s_waitcnt vmcnt(6)
	v_add_u32_e32 v18, v18, v9
	s_waitcnt vmcnt(5)
	v_add_u32_e32 v18, v18, v10
	s_waitcnt vmcnt(4)
	v_add_u32_e32 v18, v18, v11
	s_waitcnt vmcnt(3)
	v_add_u32_e32 v18, v18, v12
	s_waitcnt vmcnt(2)
	v_add_u32_e32 v18, v18, v13
	s_waitcnt vmcnt(1)
	v_add_u32_e32 v18, v18, v14
	s_waitcnt vmcnt(0)
	v_add_u32_e32 v18, v18, v15
	v_cmp_eq_u32_e32 vcc, s3, v18
	s_cbranch_vccnz .LBB0_957
	s_and_b32 s35, s34, 0xff
	s_cmp_eq_u32 s35, 0
	s_mov_b64 s[64:65], -1
	s_sleep 4
	s_cbranch_scc1 .LBB0_962
	s_and_b64 vcc, exec, s[64:65]
	s_cbranch_vccz .LBB0_957

; __device__ __forceinline__ unsigned xb_ld(unsigned* p)              { return __hip_atomic_load(p, __ATOMIC_RELAXED, __HIP_MEMORY_SCOPE_AGENT); }
; __device__ __forceinline__ unsigned xb_add(unsigned* p, unsigned v) { return __hip_atomic_fetch_add(p, v, __ATOMIC_RELAXED, __HIP_MEMORY_SCOPE_AGENT); }
; #define XB_SPIN(cond, bar) do { unsigned _sp = 0; while (cond) { __builtin_amdgcn_s_sleep(1); \
;     if ((++_sp & 255u) == 0u) { if (xb_ld(&(bar)[XB_TMO])) break; if (_sp > XB_SPIN_CAP) { atomicAdd(&(bar)[XB_TMO], 1u); break; } } } } while (0)
; __device__ __forceinline__ void xcd_barrier(const XcdBarrier& b) {
;     ...
;             const unsigned og = xb_add(&bar[XB_TOP], 1u);
;             const unsigned tg = og / nx;
;             if (og + 1u == (tg + 1u) * nx) xb_add(&bar[XB_TOPGEN], 1u);
;             else XB_SPIN(xb_ld(&bar[XB_TOPGEN]) == tg, bar);
.LBB0_974:
	s_and_b32 s34, s3, 0xff
	s_mov_b64 s[36:37], -1
	s_cmp_lg_u32 s34, 0
	s_mov_b64 s[40:41], -1
	s_sleep 4
	s_cbranch_scc0 .LBB0_977
	s_and_b64 vcc, exec, s[40:41]
	s_cbranch_vccz .LBB0_973

; __device__ __forceinline__ unsigned xb_ld(unsigned* p)              { return __hip_atomic_load(p, __ATOMIC_RELAXED, __HIP_MEMORY_SCOPE_AGENT); }
; #define XB_SPIN(cond, bar) do { unsigned _sp = 0; while (cond) { __builtin_amdgcn_s_sleep(1); \
;     if ((++_sp & 255u) == 0u) { if (xb_ld(&(bar)[XB_TMO])) break; if (_sp > XB_SPIN_CAP) { atomicAdd(&(bar)[XB_TMO], 1u); break; } } } } while (0)
; __device__ __forceinline__ void xcd_barrier(const XcdBarrier& b) {
;     ...
;         } else {
;             XB_SPIN(xb_ld(&bar[XB_XGEN(b.x)]) == gen, bar);
.LBB0_991:
	s_and_b32 s34, s3, 0xff
	s_cmp_lg_u32 s34, 0
	s_mov_b64 s[38:39], -1
	s_sleep 4
	s_cbranch_scc0 .LBB0_994
	s_mov_b64 s[40:41], -1
	s_and_b64 vcc, exec, s[38:39]
	s_cbranch_vccz .LBB0_990

; __device__ __forceinline__ unsigned xb_ld(unsigned* p)              { return __hip_atomic_load(p, __ATOMIC_RELAXED, __HIP_MEMORY_SCOPE_AGENT); }
; __device__ __forceinline__ void xcd_barrier_complete(unsigned* bar, unsigned x, unsigned& nloc, unsigned& nx) {
;     ...
;     for (;;) {
;         sum = 0u; cnt = 0u; mine = 0u;
; #pragma unroll
;         for (unsigned j = 0; j < 16; ++j) { const unsigned c = xb_ld(&bar[XB_XCNT(j)]); sum += c; cnt += (c > 0u) ? 1u : 0u; mine = (j == x) ? c : mine; }
;         if (sum == G) break;
;         __builtin_amdgcn_s_sleep(1);
;         if ((++sp & 255u) == 0u) { if (xb_ld(&bar[XB_TMO])) break; if (sp > XB_SPIN_CAP) { atomicAdd(&bar[XB_TMO], 1u); break; } }
;     }
.LBB0_1053:
	global_load_dword v16, v17, s[6:7] sc1
	global_load_dword v1, v17, s[8:9] sc1
	global_load_dword v2, v17, s[10:11] sc1
	global_load_dword v3, v17, s[12:13] sc1
	global_load_dword v4, v17, s[14:15] sc1
	global_load_dword v5, v17, s[18:19] sc1
	global_load_dword v6, v17, s[36:37] sc1
	global_load_dword v7, v17, s[38:39] sc1
	global_load_dword v8, v17, s[40:41] sc1
	global_load_dword v9, v17, s[42:43] sc1
	global_load_dword v10, v17, s[44:45] sc1
	global_load_dword v11, v17, s[46:47] sc1
	global_load_dword v12, v17, s[48:49] sc1
	global_load_dword v13, v17, s[50:51] sc1
	global_load_dword v14, v17, s[56:57] sc1
	global_load_dword v15, v17, s[58:59] sc1
	s_mov_b64 s[60:61], -1
	s_mov_b64 s[62:63], -1
	s_waitcnt vmcnt(14)
	v_add_u32_e32 v18, v1, v16
	s_waitcnt vmcnt(13)
	v_add_u32_e32 v18, v18, v2
	s_waitcnt vmcnt(12)
	v_add_u32_e32 v18, v18, v3
	s_waitcnt vmcnt(11)
	v_add_u32_e32 v18, v18, v4
	s_waitcnt vmcnt(10)
	v_add_u32_e32 v18, v18, v5
	s_waitcnt vmcnt(9)
	v_add_u32_e32 v18, v18, v6
	s_waitcnt vmcnt(8)
	v_add_u32_e32 v18, v18, v7
	s_waitcnt vmcnt(7)
	v_add_u32_e32 v18, v18, v8
	s_waitcnt vmcnt(6)
	v_add_u32_e32 v18, v18, v9
	s_waitcnt vmcnt(5)
	v_add_u32_e32 v18, v18, v10
	s_waitcnt vmcnt(4)
	v_add_u32_e32 v18, v18, v11
	s_waitcnt vmcnt(3)
	v_add_u32_e32 v18, v18, v12
	s_waitcnt vmcnt(2)
	v_add_u32_e32 v18, v18, v13
	s_waitcnt vmcnt(1)
	v_add_u32_e32 v18, v18, v14
	s_waitcnt vmcnt(0)
	v_add_u32_e32 v18, v18, v15
	v_cmp_eq_u32_e32 vcc, s34, v18
	s_cbranch_vccnz .LBB0_1052
	s_and_b32 s53, s35, 0xff
	s_cmp_eq_u32 s53, 0
	s_mov_b64 s[64:65], -1
	s_sleep 4
	s_cbranch_scc1 .LBB0_1057
	s_and_b64 vcc, exec, s[64:65]
	s_cbranch_vccz .LBB0_1052

; __device__ __forceinline__ unsigned xb_ld(unsigned* p)              { return __hip_atomic_load(p, __ATOMIC_RELAXED, __HIP_MEMORY_SCOPE_AGENT); }
; __device__ __forceinline__ unsigned xb_add(unsigned* p, unsigned v) { return __hip_atomic_fetch_add(p, v, __ATOMIC_RELAXED, __HIP_MEMORY_SCOPE_AGENT); }
; #define XB_SPIN(cond, bar) do { unsigned _sp = 0; while (cond) { __builtin_amdgcn_s_sleep(1); \
;     if ((++_sp & 255u) == 0u) { if (xb_ld(&(bar)[XB_TMO])) break; if (_sp > XB_SPIN_CAP) { atomicAdd(&(bar)[XB_TMO], 1u); break; } } } } while (0)
; __device__ __forceinline__ void xcd_barrier(const XcdBarrier& b) {
;     ...
;             const unsigned og = xb_add(&bar[XB_TOP], 1u);
;             const unsigned tg = og / nx;
;             if (og + 1u == (tg + 1u) * nx) xb_add(&bar[XB_TOPGEN], 1u);
;             else XB_SPIN(xb_ld(&bar[XB_TOPGEN]) == tg, bar);
.LBB0_1069:
	s_and_b32 s35, s34, 0xff
	s_mov_b64 s[36:37], -1
	s_cmp_lg_u32 s35, 0
	s_mov_b64 s[40:41], -1
	s_sleep 4
	s_cbranch_scc0 .LBB0_1072
	s_and_b64 vcc, exec, s[40:41]
	s_cbranch_vccz .LBB0_1068

; __device__ __forceinline__ unsigned xb_ld(unsigned* p)              { return __hip_atomic_load(p, __ATOMIC_RELAXED, __HIP_MEMORY_SCOPE_AGENT); }
; #define XB_SPIN(cond, bar) do { unsigned _sp = 0; while (cond) { __builtin_amdgcn_s_sleep(1); \
;     if ((++_sp & 255u) == 0u) { if (xb_ld(&(bar)[XB_TMO])) break; if (_sp > XB_SPIN_CAP) { atomicAdd(&(bar)[XB_TMO], 1u); break; } } } } while (0)
; __device__ __forceinline__ void xcd_barrier(const XcdBarrier& b) {
;     ...
;         } else {
;             XB_SPIN(xb_ld(&bar[XB_XGEN(b.x)]) == gen, bar);
.LBB0_1086:
	s_and_b32 s35, s34, 0xff
	s_cmp_lg_u32 s35, 0
	s_mov_b64 s[38:39], -1
	s_sleep 4
	s_cbranch_scc0 .LBB0_1089
	s_mov_b64 s[40:41], -1
	s_and_b64 vcc, exec, s[38:39]
	s_cbranch_vccz .LBB0_1085

; __device__ __forceinline__ unsigned xb_ld(unsigned* p)              { return __hip_atomic_load(p, __ATOMIC_RELAXED, __HIP_MEMORY_SCOPE_AGENT); }
; __device__ __forceinline__ void xcd_barrier_complete(unsigned* bar, unsigned x, unsigned& nloc, unsigned& nx) {
;     ...
;     for (;;) {
;         sum = 0u; cnt = 0u; mine = 0u;
; #pragma unroll
;         for (unsigned j = 0; j < 16; ++j) { const unsigned c = xb_ld(&bar[XB_XCNT(j)]); sum += c; cnt += (c > 0u) ? 1u : 0u; mine = (j == x) ? c : mine; }
;         if (sum == G) break;
;         __builtin_amdgcn_s_sleep(1);
;         if ((++sp & 255u) == 0u) { if (xb_ld(&bar[XB_TMO])) break; if (sp > XB_SPIN_CAP) { atomicAdd(&bar[XB_TMO], 1u); break; } }
;     }
.LBB0_1114:
	global_load_dword v16, v17, s[6:7] sc1
	global_load_dword v1, v17, s[8:9] sc1
	global_load_dword v2, v17, s[10:11] sc1
	global_load_dword v3, v17, s[12:13] sc1
	global_load_dword v4, v17, s[14:15] sc1
	global_load_dword v5, v17, s[16:17] sc1
	global_load_dword v6, v17, s[18:19] sc1
	global_load_dword v7, v17, s[36:37] sc1
	global_load_dword v8, v17, s[38:39] sc1
	global_load_dword v9, v17, s[40:41] sc1
	global_load_dword v10, v17, s[42:43] sc1
	global_load_dword v11, v17, s[44:45] sc1
	global_load_dword v12, v17, s[46:47] sc1
	global_load_dword v13, v17, s[48:49] sc1
	global_load_dword v14, v17, s[50:51] sc1
	global_load_dword v15, v17, s[56:57] sc1
	s_mov_b64 s[58:59], -1
	s_mov_b64 s[60:61], -1
	s_waitcnt vmcnt(14)
	v_add_u32_e32 v18, v1, v16
	s_waitcnt vmcnt(13)
	v_add_u32_e32 v18, v18, v2
	s_waitcnt vmcnt(12)
	v_add_u32_e32 v18, v18, v3
	s_waitcnt vmcnt(11)
	v_add_u32_e32 v18, v18, v4
	s_waitcnt vmcnt(10)
	v_add_u32_e32 v18, v18, v5
	s_waitcnt vmcnt(9)
	v_add_u32_e32 v18, v18, v6
	s_waitcnt vmcnt(8)
	v_add_u32_e32 v18, v18, v7
	s_waitcnt vmcnt(7)
	v_add_u32_e32 v18, v18, v8
	s_waitcnt vmcnt(6)
	v_add_u32_e32 v18, v18, v9
	s_waitcnt vmcnt(5)
	v_add_u32_e32 v18, v18, v10
	s_waitcnt vmcnt(4)
	v_add_u32_e32 v18, v18, v11
	s_waitcnt vmcnt(3)
	v_add_u32_e32 v18, v18, v12
	s_waitcnt vmcnt(2)
	v_add_u32_e32 v18, v18, v13
	s_waitcnt vmcnt(1)
	v_add_u32_e32 v18, v18, v14
	s_waitcnt vmcnt(0)
	v_add_u32_e32 v18, v18, v15
	v_cmp_eq_u32_e32 vcc, s34, v18
	s_cbranch_vccnz .LBB0_1113
	s_and_b32 s53, s35, 0xff
	s_cmp_eq_u32 s53, 0
	s_mov_b64 s[62:63], -1
	s_sleep 4
	s_cbranch_scc1 .LBB0_1118
	s_and_b64 vcc, exec, s[62:63]
	s_cbranch_vccz .LBB0_1113

; __device__ __forceinline__ unsigned xb_ld(unsigned* p)              { return __hip_atomic_load(p, __ATOMIC_RELAXED, __HIP_MEMORY_SCOPE_AGENT); }
; __device__ __forceinline__ unsigned xb_add(unsigned* p, unsigned v) { return __hip_atomic_fetch_add(p, v, __ATOMIC_RELAXED, __HIP_MEMORY_SCOPE_AGENT); }
; #define XB_SPIN(cond, bar) do { unsigned _sp = 0; while (cond) { __builtin_amdgcn_s_sleep(1); \
;     if ((++_sp & 255u) == 0u) { if (xb_ld(&(bar)[XB_TMO])) break; if (_sp > XB_SPIN_CAP) { atomicAdd(&(bar)[XB_TMO], 1u); break; } } } } while (0)
; __device__ __forceinline__ void xcd_barrier(const XcdBarrier& b) {
;     ...
;             const unsigned og = xb_add(&bar[XB_TOP], 1u);
;             const unsigned tg = og / nx;
;             if (og + 1u == (tg + 1u) * nx) xb_add(&bar[XB_TOPGEN], 1u);
;             else XB_SPIN(xb_ld(&bar[XB_TOPGEN]) == tg, bar);
.LBB0_1130:
	s_and_b32 s35, s34, 0xff
	s_mov_b64 s[18:19], -1
	s_cmp_lg_u32 s35, 0
	s_mov_b64 s[38:39], -1
	s_sleep 4
	s_cbranch_scc0 .LBB0_1133
	s_and_b64 vcc, exec, s[38:39]
	s_cbranch_vccz .LBB0_1129

; __device__ __forceinline__ unsigned xb_ld(unsigned* p)              { return __hip_atomic_load(p, __ATOMIC_RELAXED, __HIP_MEMORY_SCOPE_AGENT); }
; #define XB_SPIN(cond, bar) do { unsigned _sp = 0; while (cond) { __builtin_amdgcn_s_sleep(1); \
;     if ((++_sp & 255u) == 0u) { if (xb_ld(&(bar)[XB_TMO])) break; if (_sp > XB_SPIN_CAP) { atomicAdd(&(bar)[XB_TMO], 1u); break; } } } } while (0)
; __device__ __forceinline__ void xcd_barrier(const XcdBarrier& b) {
;     ...
;         } else {
;             XB_SPIN(xb_ld(&bar[XB_XGEN(b.x)]) == gen, bar);
.LBB0_1147:
	s_and_b32 s18, s34, 0xff
	s_cmp_lg_u32 s18, 0
	s_mov_b64 s[36:37], -1
	s_sleep 4
	s_cbranch_scc0 .LBB0_1150
	s_mov_b64 s[38:39], -1
	s_and_b64 vcc, exec, s[36:37]
	s_cbranch_vccz .LBB0_1146

; __device__ __forceinline__ unsigned xb_ld(unsigned* p)              { return __hip_atomic_load(p, __ATOMIC_RELAXED, __HIP_MEMORY_SCOPE_AGENT); }
; __device__ __forceinline__ void xcd_barrier_complete(unsigned* bar, unsigned x, unsigned& nloc, unsigned& nx) {
;     ...
;     for (;;) {
;         sum = 0u; cnt = 0u; mine = 0u;
; #pragma unroll
;         for (unsigned j = 0; j < 16; ++j) { const unsigned c = xb_ld(&bar[XB_XCNT(j)]); sum += c; cnt += (c > 0u) ? 1u : 0u; mine = (j == x) ? c : mine; }
;         if (sum == G) break;
;         __builtin_amdgcn_s_sleep(1);
;         if ((++sp & 255u) == 0u) { if (xb_ld(&bar[XB_TMO])) break; if (sp > XB_SPIN_CAP) { atomicAdd(&bar[XB_TMO], 1u); break; } }
;     }
.LBB0_1220:
	global_load_dword v16, v17, s[6:7] sc1
	global_load_dword v1, v17, s[8:9] sc1
	global_load_dword v2, v17, s[10:11] sc1
	global_load_dword v3, v17, s[12:13] sc1
	global_load_dword v4, v17, s[14:15] sc1
	global_load_dword v5, v17, s[16:17] sc1
	global_load_dword v6, v17, s[18:19] sc1
	global_load_dword v7, v17, s[20:21] sc1
	global_load_dword v8, v17, s[36:37] sc1
	global_load_dword v9, v17, s[38:39] sc1
	global_load_dword v10, v17, s[40:41] sc1
	global_load_dword v11, v17, s[42:43] sc1
	global_load_dword v12, v17, s[44:45] sc1
	global_load_dword v13, v17, s[46:47] sc1
	global_load_dword v14, v17, s[48:49] sc1
	global_load_dword v15, v17, s[50:51] sc1
	s_mov_b64 s[56:57], -1
	s_mov_b64 s[58:59], -1
	s_waitcnt vmcnt(14)
	v_add_u32_e32 v18, v1, v16
	s_waitcnt vmcnt(13)
	v_add_u32_e32 v18, v18, v2
	s_waitcnt vmcnt(12)
	v_add_u32_e32 v18, v18, v3
	s_waitcnt vmcnt(11)
	v_add_u32_e32 v18, v18, v4
	s_waitcnt vmcnt(10)
	v_add_u32_e32 v18, v18, v5
	s_waitcnt vmcnt(9)
	v_add_u32_e32 v18, v18, v6
	s_waitcnt vmcnt(8)
	v_add_u32_e32 v18, v18, v7
	s_waitcnt vmcnt(7)
	v_add_u32_e32 v18, v18, v8
	s_waitcnt vmcnt(6)
	v_add_u32_e32 v18, v18, v9
	s_waitcnt vmcnt(5)
	v_add_u32_e32 v18, v18, v10
	s_waitcnt vmcnt(4)
	v_add_u32_e32 v18, v18, v11
	s_waitcnt vmcnt(3)
	v_add_u32_e32 v18, v18, v12
	s_waitcnt vmcnt(2)
	v_add_u32_e32 v18, v18, v13
	s_waitcnt vmcnt(1)
	v_add_u32_e32 v18, v18, v14
	s_waitcnt vmcnt(0)
	v_add_u32_e32 v18, v18, v15
	v_cmp_eq_u32_e32 vcc, s34, v18
	s_cbranch_vccnz .LBB0_1219
	s_and_b32 s53, s35, 0xff
	s_cmp_eq_u32 s53, 0
	s_mov_b64 s[60:61], -1
	s_sleep 4
	s_cbranch_scc1 .LBB0_1224
	s_and_b64 vcc, exec, s[60:61]
	s_cbranch_vccz .LBB0_1219

; __device__ __forceinline__ unsigned xb_ld(unsigned* p)              { return __hip_atomic_load(p, __ATOMIC_RELAXED, __HIP_MEMORY_SCOPE_AGENT); }
; __device__ __forceinline__ unsigned xb_add(unsigned* p, unsigned v) { return __hip_atomic_fetch_add(p, v, __ATOMIC_RELAXED, __HIP_MEMORY_SCOPE_AGENT); }
; #define XB_SPIN(cond, bar) do { unsigned _sp = 0; while (cond) { __builtin_amdgcn_s_sleep(1); \
;     if ((++_sp & 255u) == 0u) { if (xb_ld(&(bar)[XB_TMO])) break; if (_sp > XB_SPIN_CAP) { atomicAdd(&(bar)[XB_TMO], 1u); break; } } } } while (0)
; __device__ __forceinline__ void xcd_barrier(const XcdBarrier& b) {
;     ...
;             const unsigned og = xb_add(&bar[XB_TOP], 1u);
;             const unsigned tg = og / nx;
;             if (og + 1u == (tg + 1u) * nx) xb_add(&bar[XB_TOPGEN], 1u);
;             else XB_SPIN(xb_ld(&bar[XB_TOPGEN]) == tg, bar);
.LBB0_1236:
	s_and_b32 s20, s34, 0xff
	s_mov_b64 s[18:19], -1
	s_cmp_lg_u32 s20, 0
	s_mov_b64 s[36:37], -1
	s_sleep 4
	s_cbranch_scc0 .LBB0_1239
	s_and_b64 vcc, exec, s[36:37]
	s_cbranch_vccz .LBB0_1235

; __device__ __forceinline__ unsigned xb_ld(unsigned* p)              { return __hip_atomic_load(p, __ATOMIC_RELAXED, __HIP_MEMORY_SCOPE_AGENT); }
; #define XB_SPIN(cond, bar) do { unsigned _sp = 0; while (cond) { __builtin_amdgcn_s_sleep(1); \
;     if ((++_sp & 255u) == 0u) { if (xb_ld(&(bar)[XB_TMO])) break; if (_sp > XB_SPIN_CAP) { atomicAdd(&(bar)[XB_TMO], 1u); break; } } } } while (0)
; __device__ __forceinline__ void xcd_barrier(const XcdBarrier& b) {
;     ...
;         } else {
;             XB_SPIN(xb_ld(&bar[XB_XGEN(b.x)]) == gen, bar);
.LBB0_1253:
	s_and_b32 s18, s34, 0xff
	s_cmp_lg_u32 s18, 0
	s_mov_b64 s[20:21], -1
	s_sleep 4
	s_cbranch_scc0 .LBB0_1256
	s_mov_b64 s[36:37], -1
	s_and_b64 vcc, exec, s[20:21]
	s_cbranch_vccz .LBB0_1252

; #define VM_WAIT() asm volatile("s_waitcnt vmcnt(0)" ::: "memory")
; __device__ __forceinline__ unsigned xb_ld(unsigned* p)              { return __hip_atomic_load(p, __ATOMIC_RELAXED, __HIP_MEMORY_SCOPE_AGENT); }
; #define XB_SPIN(cond, bar) do { unsigned _sp = 0; while (cond) { __builtin_amdgcn_s_sleep(1); \
;     if ((++_sp & 255u) == 0u) { if (xb_ld(&(bar)[XB_TMO])) break; if (_sp > XB_SPIN_CAP) { atomicAdd(&(bar)[XB_TMO], 1u); break; } } } } while (0)
; __global__ void __launch_bounds__(NTHREADS, 2) mk_fwd(Args args) {
;     ...
;                 else {
;                     if (F.tid == 0) { unsigned* bw = (unsigned*)(F.ctl + CW_BAR); XB_SPIN(xb_ld((unsigned*)(F.ctl + CW_CVT9)) < (unsigned)nconv, bw); __builtin_amdgcn_fence(__ATOMIC_ACQUIRE, "agent"); VM_WAIT(); }
;                     __syncthreads();
.LBB0_1302:
	s_and_b32 s36, s40, 0xff
	s_mov_b64 s[22:23], -1
	s_cmp_lg_u32 s36, 0
	s_mov_b64 s[38:39], -1
	s_sleep 4
	s_cbranch_scc0 .LBB0_1305
	s_and_b64 vcc, exec, s[38:39]
	s_cbranch_vccz .LBB0_1301

; __device__ __forceinline__ unsigned xb_ld(unsigned* p)              { return __hip_atomic_load(p, __ATOMIC_RELAXED, __HIP_MEMORY_SCOPE_AGENT); }
; __device__ __forceinline__ void xcd_barrier_complete(unsigned* bar, unsigned x, unsigned& nloc, unsigned& nx) {
;     ...
;     for (;;) {
;         sum = 0u; cnt = 0u; mine = 0u;
; #pragma unroll
;         for (unsigned j = 0; j < 16; ++j) { const unsigned c = xb_ld(&bar[XB_XCNT(j)]); sum += c; cnt += (c > 0u) ? 1u : 0u; mine = (j == x) ? c : mine; }
;         if (sum == G) break;
;         __builtin_amdgcn_s_sleep(1);
;         if ((++sp & 255u) == 0u) { if (xb_ld(&bar[XB_TMO])) break; if (sp > XB_SPIN_CAP) { atomicAdd(&bar[XB_TMO], 1u); break; } }
;     }
.LBB0_1356:
	global_load_dword v15, v16, s[6:7] sc1
	global_load_dword v0, v16, s[8:9] sc1
	global_load_dword v1, v16, s[10:11] sc1
	global_load_dword v2, v16, s[12:13] sc1
	global_load_dword v3, v16, s[14:15] sc1
	global_load_dword v4, v16, s[16:17] sc1
	global_load_dword v5, v16, s[18:19] sc1
	global_load_dword v6, v16, s[20:21] sc1
	global_load_dword v7, v16, s[22:23] sc1
	global_load_dword v8, v16, s[24:25] sc1
	global_load_dword v9, v16, s[36:37] sc1
	global_load_dword v10, v16, s[38:39] sc1
	global_load_dword v11, v16, s[40:41] sc1
	global_load_dword v12, v16, s[42:43] sc1
	global_load_dword v13, v16, s[44:45] sc1
	global_load_dword v14, v16, s[46:47] sc1
	s_mov_b64 s[48:49], -1
	s_mov_b64 s[50:51], -1
	s_waitcnt vmcnt(14)
	v_add_u32_e32 v17, v0, v15
	s_waitcnt vmcnt(13)
	v_add_u32_e32 v17, v17, v1
	s_waitcnt vmcnt(12)
	v_add_u32_e32 v17, v17, v2
	s_waitcnt vmcnt(11)
	v_add_u32_e32 v17, v17, v3
	s_waitcnt vmcnt(10)
	v_add_u32_e32 v17, v17, v4
	s_waitcnt vmcnt(9)
	v_add_u32_e32 v17, v17, v5
	s_waitcnt vmcnt(8)
	v_add_u32_e32 v17, v17, v6
	s_waitcnt vmcnt(7)
	v_add_u32_e32 v17, v17, v7
	s_waitcnt vmcnt(6)
	v_add_u32_e32 v17, v17, v8
	s_waitcnt vmcnt(5)
	v_add_u32_e32 v17, v17, v9
	s_waitcnt vmcnt(4)
	v_add_u32_e32 v17, v17, v10
	s_waitcnt vmcnt(3)
	v_add_u32_e32 v17, v17, v11
	s_waitcnt vmcnt(2)
	v_add_u32_e32 v17, v17, v12
	s_waitcnt vmcnt(1)
	v_add_u32_e32 v17, v17, v13
	s_waitcnt vmcnt(0)
	v_add_u32_e32 v17, v17, v14
	v_cmp_eq_u32_e32 vcc, s34, v17
	s_cbranch_vccnz .LBB0_1355
	s_and_b32 s48, s35, 0xff
	s_cmp_eq_u32 s48, 0
	s_mov_b64 s[48:49], -1
	s_mov_b64 s[54:55], -1
	s_sleep 4
	s_cbranch_scc1 .LBB0_1360
	s_and_b64 vcc, exec, s[54:55]
	s_cbranch_vccz .LBB0_1355

; __device__ __forceinline__ unsigned xb_ld(unsigned* p)              { return __hip_atomic_load(p, __ATOMIC_RELAXED, __HIP_MEMORY_SCOPE_AGENT); }
; __device__ __forceinline__ unsigned xb_add(unsigned* p, unsigned v) { return __hip_atomic_fetch_add(p, v, __ATOMIC_RELAXED, __HIP_MEMORY_SCOPE_AGENT); }
; #define XB_SPIN(cond, bar) do { unsigned _sp = 0; while (cond) { __builtin_amdgcn_s_sleep(1); \
;     if ((++_sp & 255u) == 0u) { if (xb_ld(&(bar)[XB_TMO])) break; if (_sp > XB_SPIN_CAP) { atomicAdd(&(bar)[XB_TMO], 1u); break; } } } } while (0)
; __device__ __forceinline__ void xcd_barrier(const XcdBarrier& b) {
;     ...
;             const unsigned og = xb_add(&bar[XB_TOP], 1u);
;             const unsigned tg = og / nx;
;             if (og + 1u == (tg + 1u) * nx) xb_add(&bar[XB_TOPGEN], 1u);
;             else XB_SPIN(xb_ld(&bar[XB_TOPGEN]) == tg, bar);
.LBB0_1372:
	s_and_b32 s20, s24, 0xff
	s_mov_b64 s[18:19], -1
	s_cmp_lg_u32 s20, 0
	s_mov_b64 s[22:23], -1
	s_sleep 4
	s_cbranch_scc0 .LBB0_1375
	s_and_b64 vcc, exec, s[22:23]
	s_cbranch_vccz .LBB0_1371

; __device__ __forceinline__ unsigned xb_ld(unsigned* p)              { return __hip_atomic_load(p, __ATOMIC_RELAXED, __HIP_MEMORY_SCOPE_AGENT); }
; #define XB_SPIN(cond, bar) do { unsigned _sp = 0; while (cond) { __builtin_amdgcn_s_sleep(1); \
;     if ((++_sp & 255u) == 0u) { if (xb_ld(&(bar)[XB_TMO])) break; if (_sp > XB_SPIN_CAP) { atomicAdd(&(bar)[XB_TMO], 1u); break; } } } } while (0)
; __device__ __forceinline__ void xcd_barrier(const XcdBarrier& b) {
;     ...
;         } else {
;             XB_SPIN(xb_ld(&bar[XB_XGEN(b.x)]) == gen, bar);
.LBB0_1389:
	s_and_b32 s18, s24, 0xff
	s_cmp_lg_u32 s18, 0
	s_mov_b64 s[20:21], -1
	s_sleep 4
	s_cbranch_scc0 .LBB0_1392
	s_mov_b64 s[22:23], -1
	s_and_b64 vcc, exec, s[20:21]
	s_cbranch_vccz .LBB0_1388
